# v4 + mLSTM chain: store acks not awaited in the chunk loop (vmcnt +8), barrier A before the prefetch issue
# baseline (speedup 1.0000x reference)
.LBB0_2127:
	s_or_b64 exec, exec, s[0:1]
	v_readlane_b32 s19, v254, 51
	s_bfe_u32 s33, s19, 0x20006
	s_lshl_b32 s1, s90, 6
	s_lshl_b32 s2, s33, 4
	s_ashr_i32 s0, s90, 3
	s_and_b32 s7, s1, 0x1c0
	s_cmp_eq_u32 s7, 0
	s_cselect_b64 s[38:39], -1, 0
	s_lshl_b32 s4, s0, 8
	s_ashr_i32 s5, s4, 31
	s_lshl_b64 s[4:5], s[4:5], 1
	s_add_u32 s1, s30, s4
	s_addc_u32 s4, s31, s5
	s_add_u32 s44, s1, 0xd100000
	s_addc_u32 s5, s4, 0
	s_and_b32 s45, s5, 0xffff
	s_add_u32 s48, s1, 0xb100000
	s_addc_u32 s1, s4, 0
	s_lshl_b32 s4, s0, 9
	s_and_b32 s49, s1, 0xffff
	s_or_b32 s1, s4, s7
	s_lshl_b32 s1, s1, 1
	s_sub_i32 s6, 0x1dbfb200, s1
	s_ashr_i32 s1, s0, 31
	s_ashr_i32 s5, s4, 31
	s_lshl_b64 s[8:9], s[0:1], 20
	s_add_u32 s8, s30, s8
	s_addc_u32 s9, s31, s9
	s_add_u32 s52, s8, 0x6a400000
	s_addc_u32 s12, s9, 0
	s_lshl_b64 s[8:9], s[4:5], 2
	s_add_u32 s8, s30, s8
	s_addc_u32 s9, s31, s9
	s_lshl_b32 s10, s7, 2
	s_add_u32 s8, s8, s10
	s_addc_u32 s9, s9, 0
	s_add_u32 s40, s8, 0x6ad00000
	s_addc_u32 s10, s9, 0
	s_lshl_b64 s[8:9], s[0:1], 2
	s_add_u32 s8, s30, s8
	v_and_b32_e32 v4, 7, v152
	s_addc_u32 s9, s31, s9
	v_mov_b32_e32 v5, 0x3f80
	v_cmp_eq_u32_e32 vcc, 0, v4
	s_add_u32 s20, s8, 0xa880000
	v_mov_b32_e32 v151, 0
	v_cndmask_b32_e32 v5, 0, v5, vcc
	s_addc_u32 s18, s9, 0
	s_and_b32 s70, s19, 0xffffff00
	s_lshl_b64 s[0:1], s[0:1], 15
	ds_write2st64_b32 v2, v5, v151 offset0:240 offset1:248
	v_lshlrev_b32_e32 v5, 4, v152
	s_add_u32 s0, s30, s0
	v_lshrrev_b32_e32 v3, 4, v1
	v_and_b32_e32 v6, 15, v152
	v_lshlrev_b32_e32 v2, 7, v152
	v_and_b32_e32 v8, 0x1f0, v5
	s_movk_i32 s8, 0xf000
	s_addc_u32 s1, s31, s1
	s_mov_b32 s47, 0x20000
	s_brev_b32 s46, 64
	v_and_or_b32 v162, v2, s8, v8
	v_or_b32_e32 v5, s2, v6
	v_lshl_or_b32 v11, v3, 2, s2
	s_add_u32 s8, s0, 0x6ac40000
	s_mov_b32 s2, 0x10000
	s_addc_u32 s9, s1, 0
	buffer_load_dwordx4 v[58:61], v162, s[44:47], 0 offen
	buffer_load_dwordx4 v[62:65], v162, s[44:47], s2 offen
	s_mov_b32 s2, 0x30000
	s_lshl_b64 s[4:5], s[4:5], 1
	buffer_load_dwordx4 v[66:69], v162, s[44:47], s47 offen
	buffer_load_dwordx4 v[70:73], v162, s[44:47], s2 offen
	s_add_u32 s2, s30, s4
	s_addc_u32 s4, s31, s5
	s_lshl_b32 s5, s7, 1
	s_add_u32 s2, s2, s5
	s_addc_u32 s5, s4, 0
	s_add_u32 s4, s2, 0x29f04e00
	v_and_b32_e32 v9, 48, v152
	s_addc_u32 s2, s5, 0
	v_ashrrev_i32_e32 v2, 3, v152
	v_or_b32_e32 v10, s70, v9
	v_lshlrev_b32_e32 v12, 2, v6
	s_and_b32 s5, s2, 0xffff
	s_and_b32 s41, s10, 0xffff
	s_mov_b32 s2, 0xee00
	v_or_b32_e32 v7, s7, v4
	s_mov_b32 s50, s46
	s_mov_b32 s51, s47
	v_lshlrev_b32_e32 v4, 4, v4
	v_lshl_or_b32 v158, v11, 14, v12
	v_mul_lo_u32 v12, v2, s2
	v_lshl_add_u32 v165, v5, 12, v10
	s_add_u32 s10, s0, 0x6ac80000
	s_movk_i32 s2, 0x80
	s_mov_b32 s7, s47
	v_or_b32_e32 v164, v12, v4
	s_addc_u32 s11, s1, 0
	buffer_load_dwordx4 v[110:113], v165, s[48:51], 0 offen
	s_waitcnt lgkmcnt(1)
	buffer_load_dwordx4 v[130:133], v165, s[48:51], 64 offen
	s_movk_i32 s13, 0xc0
	buffer_load_dwordx4 v[138:141], v165, s[48:51], s2 offen
	buffer_load_dwordx4 v[134:137], v165, s[48:51], s13 offen
	s_and_b32 s53, s12, 0xffff
	s_mov_b32 s12, s52
	s_movk_i32 s2, 0x90
	s_mov_b32 s56, s4
	s_mov_b32 s57, s5
	s_mov_b32 s14, 0x100000
	s_mov_b32 s13, s53
	s_mov_b32 s15, s47
	s_and_b32 s21, s18, 0xffff
	v_lshl_or_b32 v167, v5, 7, v9
	buffer_load_dwordx4 v[74:77], v164, s[4:7], 0 offen
	buffer_load_dwordx4 v[106:109], v167, s[12:15], 0 offen
	buffer_load_dwordx4 v[102:105], v167, s[12:15], 64 offen
	v_mad_u64_u32 v[154:155], s[4:5], v2, s2, v[4:5]
	s_lshl_b32 s12, s33, 6
	s_add_u32 s4, s10, s12
	s_addc_u32 s5, s11, 0
	s_mov_b32 s58, s6
	v_lshlrev_b32_e32 v10, 3, v3
	v_and_b32_e32 v3, 48, v1
	s_add_u32 s6, s8, s12
	s_addc_u32 s7, s9, 0
	global_load_dwordx4 v[98:101], v3, s[4:5]
	global_load_dwordx4 v[94:97], v3, s[6:7]
	v_ashrrev_i32_e32 v3, 31, v2
	v_lshlrev_b64 v[156:157], 2, v[2:3]
	v_lshl_add_u64 v[4:5], s[0:1], 0, v[156:157]
	s_mov_b32 s2, 0x6ac00000
	v_add_co_u32_e32 v4, vcc, s2, v4
	s_cmp_lt_u32 s68, 4
	s_nop 0
	v_addc_co_u32_e32 v5, vcc, 0, v5, vcc
	global_load_dword v176, v[4:5], off
	global_load_dword v170, v151, s[8:9] offset:252
	global_load_dword v177, v151, s[10:11] offset:252
	s_cselect_b64 s[60:61], -1, 0
	s_cmp_gt_u32 s68, 3
	s_cselect_b64 s[62:63], -1, 0
	s_add_i32 s2, 0, 0x10000
	v_lshlrev_b32_e32 v166, 5, v2
	s_movk_i32 s6, 0x210
	v_mov_b32_e32 v2, s2
	v_ashrrev_i32_e32 v4, 5, v152
	v_mad_u32_u24 v2, v6, s6, v2
	v_cmp_eq_u32_e32 vcc, 0, v6
	v_mul_lo_u32 v6, v4, s6
	v_add_u32_e32 v4, 0x200, v152
	v_ashrrev_i32_e32 v4, 5, v4
	v_lshlrev_b32_e32 v153, 5, v11
	s_add_i32 s2, 0, 0x1a500
	s_and_b32 s7, s19, 0xffffffc0
	v_mul_lo_u32 v11, v4, s6
	v_add_u32_e32 v4, 0x400, v152
	s_and_b64 s[64:65], s[38:39], s[60:61]
	v_lshl_add_u32 v155, v1, 4, s2
	s_add_i32 s2, s7, 0
	v_ashrrev_i32_e32 v4, 5, v4
	v_mul_lo_u32 v12, v4, s6
	v_add_u32_e32 v4, 0x600, v152
	s_cmpk_eq_i32 s70, 0x100
	v_bfe_u32 v3, v152, 2, 2
	v_lshlrev_b32_e32 v1, 3, v1
	v_ashrrev_i32_e32 v4, 5, v4
	s_cselect_b64 s[66:67], -1, 0
	s_cmpk_lg_i32 s70, 0x100
	v_add_u32_e32 v8, 0, v8
	v_cmp_eq_u32_e64 s[4:5], 0, v7
	v_add_u32_e32 v7, v2, v9
	v_or_b32_e32 v3, v10, v3
	v_and_b32_e32 v169, 24, v1
	v_mul_lo_u32 v13, v4, s6
	s_cselect_b64 s[74:75], -1, 0
	s_and_b64 s[18:19], s[64:65], vcc
	v_mov_b32_e32 v4, v151
	v_mov_b32_e32 v5, v151
	v_add_u32_e32 v1, s2, v169
	v_mul_u32_u24_e32 v14, 0x210, v3
	v_mul_u32_u24_e32 v171, 0x90, v3
	v_lshlrev_b32_e32 v152, 5, v3
	v_add_u32_e32 v15, s7, v2
	s_add_u32 s76, s0, 0x6ac801fc
	v_or_b32_e32 v150, s12, v9
	v_mov_b32_e32 v2, v151
	v_mov_b32_e32 v3, v151
	v_add_u32_e32 v172, v8, v6
	v_add_u32_e32 v173, v8, v11
	v_add_u32_e32 v174, v8, v12
	v_add_u32_e32 v175, v8, v13
	v_add_u32_e32 v163, s70, v7
	v_mov_b64_e32 v[8:9], v[4:5]
	s_mov_b32 s3, 0
	s_mov_b32 s59, s47
	s_brev_b32 s42, 16
	s_mov_b32 s43, s47
	s_mov_b32 s54, s14
	s_mov_b32 s55, s47
	s_mov_b32 s22, 0x40000
	s_mov_b32 s23, s47
	v_add_u32_e32 v159, 0, v169
	s_mulk_i32 s33, 0x1400
	s_mul_i32 s2, s68, 0x1400
	s_addc_u32 s77, s1, 0
	s_movk_i32 s34, 0x60
	s_mov_b32 s35, 0x70000
	s_movk_i32 s36, 0x2040
	s_mov_b32 s37, 0x3b8000
	s_mov_b32 s68, 0xfffc0000
	s_mov_b32 s69, 0xfff80000
	v_add_u32_e32 v161, v1, v14
	v_add_u32_e32 v1, v15, v10
	v_mov_b64_e32 v[6:7], v[2:3]
	v_mov_b32_e32 v160, v151
	s_mov_b32 s70, 0
	v_mov_b32_e32 v54, v151
	v_mov_b32_e32 v55, v151
	v_mov_b32_e32 v56, v151
	v_mov_b32_e32 v57, v151
	v_mov_b32_e32 v38, v151
	v_mov_b32_e32 v39, v151
	v_mov_b32_e32 v40, v151
	v_mov_b32_e32 v41, v151
	v_mov_b32_e32 v30, v151
	v_mov_b32_e32 v31, v151
	v_mov_b32_e32 v32, v151
	v_mov_b32_e32 v33, v151
	v_mov_b32_e32 v26, v151
	v_mov_b32_e32 v27, v151
	v_mov_b32_e32 v28, v151
	v_mov_b32_e32 v29, v151
	v_mov_b32_e32 v50, v151
	v_mov_b32_e32 v51, v151
	v_mov_b32_e32 v52, v151
	v_mov_b32_e32 v53, v151
	v_mov_b32_e32 v46, v151
	v_mov_b32_e32 v47, v151
	v_mov_b32_e32 v48, v151
	v_mov_b32_e32 v49, v151
	v_mov_b32_e32 v42, v151
	v_mov_b32_e32 v43, v151
	v_mov_b32_e32 v44, v151
	v_mov_b32_e32 v45, v151
	v_mov_b32_e32 v34, v151
	v_mov_b32_e32 v35, v151
	v_mov_b32_e32 v36, v151
	v_mov_b32_e32 v37, v151
	s_waitcnt vmcnt(0)
.LBB0_2128:
	v_max_f32_e32 v10, v177, v177
	v_max_f32_e32 v181, v160, v160
	v_max_f32_e32 v179, v181, v10
	v_sub_f32_e32 v10, v176, v179
	v_mul_f32_e32 v10, 0x3fb8aa3b, v10
	v_exp_f32_e32 v10, v10
	s_bitcmp1_b32 s70, 0
	s_cselect_b32 s0, 0x2400, 0
	s_add_i32 s6, s0, 0
	v_add_u32_e32 v11, s6, v154
	v_lshlrev_b32_e32 v12, 16, v74
	v_and_b32_e32 v13, 0xffff0000, v74
	v_lshlrev_b32_e32 v14, 16, v75
	v_and_b32_e32 v15, 0xffff0000, v75
	v_lshlrev_b32_e32 v16, 16, v76
	v_and_b32_e32 v17, 0xffff0000, v76
	v_lshlrev_b32_e32 v18, 16, v77
	v_and_b32_e32 v19, 0xffff0000, v77
	v_pk_mul_f32 v[14:15], v[10:11], v[14:15] op_sel_hi:[0,1]
	v_pk_mul_f32 v[12:13], v[10:11], v[12:13] op_sel_hi:[0,1]
	v_pk_mul_f32 v[18:19], v[10:11], v[18:19] op_sel_hi:[0,1]
	v_pk_mul_f32 v[16:17], v[10:11], v[16:17] op_sel_hi:[0,1]
	v_cvt_pk_bf16_f32 v12, v12, v13
	v_cvt_pk_bf16_f32 v13, v14, v15
	v_cvt_pk_bf16_f32 v14, v16, v17
	v_cvt_pk_bf16_f32 v15, v18, v19
	v_add_u32_e32 v178, 0, v154
	ds_write_b128 v172, v[58:61]
	ds_write_b128 v173, v[62:65]
	ds_write_b128 v174, v[66:69]
	ds_write_b128 v175, v[70:73]
	ds_write_b128 v11, v[74:77] offset:33792
	ds_write_b128 v178, v[12:15] offset:52224
	s_and_saveexec_b64 s[0:1], s[4:5]
	v_cvt_pk_bf16_f32 v10, v10, s0
	v_add_u32_e32 v11, 0, v166
	ds_write_b16 v11, v10 offset:63488
	s_or_b64 exec, exec, s[0:1]
	s_waitcnt lgkmcnt(0)
	s_barrier
	s_add_i32 s0, s35, 0xfffd0000
	s_add_i32 s1, s35, 0xfffe0000
	v_lshl_add_u64 v[10:11], s[76:77], 0, v[150:151]
	buffer_load_dwordx4 v[58:61], v162, s[44:47], s0 offen
	buffer_load_dwordx4 v[62:65], v162, s[44:47], s1 offen
	s_add_i32 s1, s35, 0xffff0000
	s_mov_b32 s50, s46
	s_mov_b32 s51, s47
	v_add_co_u32_e32 v12, vcc, s68, v10
	buffer_load_dwordx4 v[66:69], v162, s[44:47], s1 offen
	buffer_load_dwordx4 v[70:73], v162, s[44:47], s35 offen
	s_add_i32 s1, s35, 0xfffd0040
	buffer_load_dwordx4 v[90:93], v165, s[48:51], s0 offen
	buffer_load_dwordx4 v[82:85], v165, s[48:51], s1 offen
	s_add_i32 s0, s35, 0xfffd0080
	v_addc_co_u32_e32 v13, vcc, -1, v11, vcc
	v_lshl_add_u64 v[114:115], s[76:77], 0, v[156:157]
	s_add_i32 s1, s35, 0xfffd00c0
	buffer_load_dwordx4 v[86:89], v165, s[48:51], s0 offen
	buffer_load_dwordx4 v[78:81], v165, s[48:51], s1 offen
	s_sub_i32 s0, s36, 64
	v_add_co_u32_e32 v114, vcc, s69, v114
	buffer_load_dwordx4 v[74:77], v164, s[56:59], s37 offen
	buffer_load_dwordx4 v[22:25], v167, s[52:55], s0 offen
	buffer_load_dwordx4 v[18:21], v167, s[52:55], s36 offen
	v_addc_co_u32_e32 v115, vcc, -1, v115, vcc
	s_add_u32 s0, s76, 0xfffc0000
	global_load_dwordx4 v[14:17], v[10:11], off offset:-252
	s_nop 0
	global_load_dwordx4 v[10:13], v[12:13], off offset:-252
	s_addc_u32 s1, s77, -1
	global_load_dword v176, v[114:115], off offset:-252
	global_load_dword v180, v151, s[0:1]
	global_load_dword v177, v151, s[76:77]
	ds_read_b128 v[114:117], v163
	ds_read_b128 v[118:121], v163 offset:64
	s_waitcnt lgkmcnt(1)
	v_mfma_f32_16x16x32_bf16 v[114:117], v[110:113], v[114:117], 0
	s_andn2_b64 vcc, exec, s[62:63]
	s_waitcnt lgkmcnt(0)
	v_mfma_f32_16x16x32_bf16 v[114:117], v[130:133], v[118:121], v[114:117]
	ds_read_b128 v[118:121], v163 offset:128
	ds_read_b128 v[122:125], v163 offset:192
	s_waitcnt lgkmcnt(1)
	v_mfma_f32_16x16x32_bf16 v[114:117], v[138:141], v[118:121], v[114:117]
	v_cndmask_b32_e64 v118, 0, 1, s[62:63]
	v_cmp_ne_u32_e64 s[10:11], 1, v118
	s_waitcnt lgkmcnt(0)
	v_mfma_f32_16x16x32_bf16 v[126:129], v[134:137], v[122:125], v[114:117]
	s_cbranch_vccnz .LBB0_2132
	s_nop 2
	v_add_u32_e32 v114, s33, v155
	s_nop 2
	ds_write_b128 v114, v[126:129]

.LBB0_2160:
	s_add_i32 s3, s3, 0x100000
	s_addk_i32 s34, 0x800
	s_add_i32 s35, s35, 0x40000
	s_add_u32 s76, s76, 0x100
	s_addc_u32 s77, s77, 0
	s_addk_i32 s36, 0x2000
	s_add_i32 s37, s37, 0x3b8000
	s_add_i32 s70, s70, 1
	s_cmp_lg_u32 s3, 0x7f00000
	v_add_f32_e32 v160, v170, v179
	s_cbranch_scc0 .LBB0_2164
	s_waitcnt vmcnt(14)
	v_mov_b64_e32 v[108:109], v[24:25]
	s_waitcnt vmcnt(13)
	v_mov_b64_e32 v[104:105], v[20:21]
	v_mov_b64_e32 v[112:113], v[92:93]
	v_mov_b64_e32 v[132:133], v[84:85]
	v_mov_b64_e32 v[140:141], v[88:89]
	v_mov_b64_e32 v[136:137], v[80:81]
	s_waitcnt vmcnt(12)
	v_mov_b64_e32 v[100:101], v[16:17]
	s_waitcnt vmcnt(11)
	v_mov_b64_e32 v[96:97], v[12:13]
	v_mov_b64_e32 v[106:107], v[22:23]
	v_mov_b64_e32 v[102:103], v[18:19]
	v_mov_b64_e32 v[110:111], v[90:91]
	v_mov_b64_e32 v[130:131], v[82:83]
	v_mov_b64_e32 v[138:139], v[86:87]
	v_mov_b64_e32 v[134:135], v[78:79]
	v_mov_b64_e32 v[98:99], v[14:15]
	v_mov_b64_e32 v[94:95], v[10:11]
	s_waitcnt vmcnt(9)
	v_mov_b32_e32 v170, v180
	s_waitcnt vmcnt(8)
	s_branch .LBB0_2128
